# speedup vs baseline: 1.0052x; 1.0052x over previous
.Lskip_issueB:
	s_mov_b64 exec, -1
	s_barrier
	s_mov_b64 exec, s[30:31]
	ds_read_b128 v[20:23], v5 offset:32768
	s_mov_b64 exec, s[32:33]
	ds_read_b128 v[56:59], v42 offset:40960
	s_cmp_eq_u64 s[32:33], 0
	s_cbranch_scc1 .Lwait_all
	s_waitcnt vmcnt(2)
	s_branch .Lwait_done

.Lwait_done:
	s_mov_b64 exec, s[30:31]
	s_cbranch_execz .Lskip_compA
	s_waitcnt lgkmcnt(0)
	v_pk_add_f32 v[8:9], v[22:23], v[20:21] neg_lo:[0,1] neg_hi:[0,1]
	s_nop 0
	v_pk_fma_f32 v[20:21], v[8:9], 0.5, v[20:21] op_sel_hi:[1,0,1]
	v_mul_f32_e32 v5, 0x3fb8aa3b, v14
	v_mul_f32_e32 v7, 0x3fb8aa3b, v15
	v_pk_fma_f32 v[12:13], v[12:13], v[8:9], v[20:21]
	v_sub_f32_e32 v14, v18, v16
	v_sub_f32_e32 v20, v19, v17
	v_max_f32_e32 v11, v18, v18
	v_max_f32_e32 v15, v16, v16
	v_max_f32_e32 v18, v19, v19
	v_max_f32_e32 v19, v17, v17
	v_exp_f32_e32 v16, v5
	v_exp_f32_e32 v17, v7
	s_nop 0
	v_pk_mul_f32 v[8:9], v[16:17], v[8:9]
	s_nop 0
	v_pk_fma_f32 v[16:17], v[8:9], 0.5, v[12:13] op_sel_hi:[1,0,1] neg_lo:[1,0,0] neg_hi:[1,0,0]
	v_pk_fma_f32 v[8:9], v[8:9], 0.5, v[12:13] op_sel_hi:[1,0,1]
	v_max_f32_e32 v7, v16, v15
	v_min_f32_e32 v5, v8, v11
	v_min_f32_e32 v21, v9, v18
	v_max_f32_e32 v22, v17, v19
	v_pk_add_f32 v[12:13], v[8:9], v[16:17] neg_lo:[0,1] neg_hi:[0,1]
	v_max_f32_e32 v8, v8, v11
	v_min_f32_e32 v11, v16, v15
	v_max_f32_e32 v9, v9, v18
	v_min_f32_e32 v15, v17, v19
	v_sub_f32_e32 v5, v5, v7
	v_sub_f32_e32 v7, v21, v22
	v_sub_f32_e32 v8, v8, v11
	v_sub_f32_e32 v9, v9, v15
	v_max_f32_e32 v15, 0, v5
	v_max_f32_e32 v21, 0, v7
	v_max_f32_e32 v5, 0, v8
	v_max_f32_e32 v7, 0, v9
	v_pk_mul_f32 v[8:9], v[14:15], v[20:21]
	v_mul_f32_e32 v11, v5, v7
	v_fma_f32 v8, v12, v13, v8
	v_sub_f32_e32 v8, v8, v9
	v_rcp_f32_e32 v14, v11
	v_rcp_f32_e32 v15, v8
	v_fma_f32 v8, v5, v7, -v8
	v_pk_mul_f32 v[8:9], v[14:15], v[8:9]
	s_nop 0
	v_sub_f32_e32 v5, v8, v9
	v_add_f32_e32 v5, 1.0, v5
	v_add_f32_e32 v2, v2, v5
.Lskip_compA:
	s_waitcnt vmcnt(0) lgkmcnt(0)
	s_mov_b64 exec, s[32:33]
	s_cbranch_execz .Lskip_compB
	v_mov_b32_e32 v12, v34
	v_mov_b32_e32 v13, v35
	v_mov_b32_e32 v14, v36
	v_mov_b32_e32 v15, v37
	v_mov_b32_e32 v16, v38
	v_mov_b32_e32 v17, v39
	v_mov_b32_e32 v18, v40
	v_mov_b32_e32 v19, v41
	v_mov_b32_e32 v20, v56
	v_mov_b32_e32 v21, v57
	v_mov_b32_e32 v22, v58
	v_mov_b32_e32 v23, v59
	s_waitcnt lgkmcnt(0)
	v_pk_add_f32 v[8:9], v[22:23], v[20:21] neg_lo:[0,1] neg_hi:[0,1]
	s_nop 0
	v_pk_fma_f32 v[20:21], v[8:9], 0.5, v[20:21] op_sel_hi:[1,0,1]
	v_mul_f32_e32 v5, 0x3fb8aa3b, v14
	v_mul_f32_e32 v7, 0x3fb8aa3b, v15
	v_pk_fma_f32 v[12:13], v[12:13], v[8:9], v[20:21]
	v_sub_f32_e32 v14, v18, v16
	v_sub_f32_e32 v20, v19, v17
	v_max_f32_e32 v11, v18, v18
	v_max_f32_e32 v15, v16, v16
	v_max_f32_e32 v18, v19, v19
	v_max_f32_e32 v19, v17, v17
	v_exp_f32_e32 v16, v5
	v_exp_f32_e32 v17, v7
	s_nop 0
	v_pk_mul_f32 v[8:9], v[16:17], v[8:9]
	s_nop 0
	v_pk_fma_f32 v[16:17], v[8:9], 0.5, v[12:13] op_sel_hi:[1,0,1] neg_lo:[1,0,0] neg_hi:[1,0,0]
	v_pk_fma_f32 v[8:9], v[8:9], 0.5, v[12:13] op_sel_hi:[1,0,1]
	v_max_f32_e32 v7, v16, v15
	v_min_f32_e32 v5, v8, v11
	v_min_f32_e32 v21, v9, v18
	v_max_f32_e32 v22, v17, v19
	v_pk_add_f32 v[12:13], v[8:9], v[16:17] neg_lo:[0,1] neg_hi:[0,1]
	v_max_f32_e32 v8, v8, v11
	v_min_f32_e32 v11, v16, v15
	v_max_f32_e32 v9, v9, v18
	v_min_f32_e32 v15, v17, v19
	v_sub_f32_e32 v5, v5, v7
	v_sub_f32_e32 v7, v21, v22
	v_sub_f32_e32 v8, v8, v11
	v_sub_f32_e32 v9, v9, v15
	v_max_f32_e32 v15, 0, v5
	v_max_f32_e32 v21, 0, v7
	v_max_f32_e32 v5, 0, v8
	v_max_f32_e32 v7, 0, v9
	v_pk_mul_f32 v[8:9], v[14:15], v[20:21]
	v_mul_f32_e32 v11, v5, v7
	v_fma_f32 v8, v12, v13, v8
	v_sub_f32_e32 v8, v8, v9
	v_rcp_f32_e32 v14, v11
	v_rcp_f32_e32 v15, v8
	v_fma_f32 v8, v5, v7, -v8
	v_pk_mul_f32 v[8:9], v[14:15], v[8:9]
	s_nop 0
	v_sub_f32_e32 v5, v8, v9
	v_add_f32_e32 v5, 1.0, v5
	v_add_f32_e32 v2, v2, v5

	.amdhsa_kernel _Z12giou_partialPK15HIP_vector_typeIfLj4EES2_S2_PKiPS_IfLj2EE
		.amdhsa_group_segment_fixed_size 49280
		.amdhsa_private_segment_fixed_size 0
		.amdhsa_kernarg_size 40
		.amdhsa_user_sgpr_count 2
		.amdhsa_user_sgpr_dispatch_ptr 0
		.amdhsa_user_sgpr_queue_ptr 0
		.amdhsa_user_sgpr_kernarg_segment_ptr 1
		.amdhsa_user_sgpr_dispatch_id 0
		.amdhsa_user_sgpr_kernarg_preload_length 0
		.amdhsa_user_sgpr_kernarg_preload_offset 0
		.amdhsa_user_sgpr_private_segment_size 0
		.amdhsa_uses_dynamic_stack 0
		.amdhsa_enable_private_segment 0
		.amdhsa_system_sgpr_workgroup_id_x 1
		.amdhsa_system_sgpr_workgroup_id_y 0
		.amdhsa_system_sgpr_workgroup_id_z 0
		.amdhsa_system_sgpr_workgroup_info 0
		.amdhsa_system_vgpr_workitem_id 0
		.amdhsa_next_free_vgpr 60
		.amdhsa_next_free_sgpr 34
		.amdhsa_accum_offset 60
		.amdhsa_reserve_vcc 1
		.amdhsa_float_round_mode_32 0
		.amdhsa_float_round_mode_16_64 0
		.amdhsa_float_denorm_mode_32 3
		.amdhsa_float_denorm_mode_16_64 3
		.amdhsa_dx10_clamp 1
		.amdhsa_ieee_mode 1
		.amdhsa_fp16_overflow 0
		.amdhsa_tg_split 0
		.amdhsa_exception_fp_ieee_invalid_op 0
		.amdhsa_exception_fp_denorm_src 0
		.amdhsa_exception_fp_ieee_div_zero 0
		.amdhsa_exception_fp_ieee_overflow 0
		.amdhsa_exception_fp_ieee_underflow 0
		.amdhsa_exception_fp_ieee_inexact 0
		.amdhsa_exception_int_div_zero 0
	.end_amdhsa_kernel

.Lfunc_end0:
	.size	_Z12giou_partialPK15HIP_vector_typeIfLj4EES2_S2_PKiPS_IfLj2EE, .Lfunc_end0-_Z12giou_partialPK15HIP_vector_typeIfLj4EES2_S2_PKiPS_IfLj2EE
	.set _Z12giou_partialPK15HIP_vector_typeIfLj4EES2_S2_PKiPS_IfLj2EE.num_vgpr, 60
	.set _Z12giou_partialPK15HIP_vector_typeIfLj4EES2_S2_PKiPS_IfLj2EE.num_agpr, 0
	.set _Z12giou_partialPK15HIP_vector_typeIfLj4EES2_S2_PKiPS_IfLj2EE.numbered_sgpr, 34
	.set _Z12giou_partialPK15HIP_vector_typeIfLj4EES2_S2_PKiPS_IfLj2EE.num_named_barrier, 0
	.set _Z12giou_partialPK15HIP_vector_typeIfLj4EES2_S2_PKiPS_IfLj2EE.private_seg_size, 0
	.set _Z12giou_partialPK15HIP_vector_typeIfLj4EES2_S2_PKiPS_IfLj2EE.uses_vcc, 1
	.set _Z12giou_partialPK15HIP_vector_typeIfLj4EES2_S2_PKiPS_IfLj2EE.uses_flat_scratch, 0
	.set _Z12giou_partialPK15HIP_vector_typeIfLj4EES2_S2_PKiPS_IfLj2EE.has_dyn_sized_stack, 0
	.set _Z12giou_partialPK15HIP_vector_typeIfLj4EES2_S2_PKiPS_IfLj2EE.has_recursion, 0
	.set _Z12giou_partialPK15HIP_vector_typeIfLj4EES2_S2_PKiPS_IfLj2EE.has_indirect_call, 0

amdhsa.kernels:
  - .agpr_count:     0
    .args:
      - .actual_access:  read_only
        .address_space:  global
        .offset:         0
        .size:           8
        .value_kind:     global_buffer
      - .actual_access:  read_only
        .address_space:  global
        .offset:         8
        .size:           8
        .value_kind:     global_buffer
      - .actual_access:  read_only
        .address_space:  global
        .offset:         16
        .size:           8
        .value_kind:     global_buffer
      - .actual_access:  read_only
        .address_space:  global
        .offset:         24
        .size:           8
        .value_kind:     global_buffer
      - .actual_access:  write_only
        .address_space:  global
        .offset:         32
        .size:           8
        .value_kind:     global_buffer
    .group_segment_fixed_size: 49280
    .kernarg_segment_align: 8
    .kernarg_segment_size: 40
    .language:       OpenCL C
    .language_version:
      - 2
      - 0
    .max_flat_workgroup_size: 1024
    .name:           _Z12giou_partialPK15HIP_vector_typeIfLj4EES2_S2_PKiPS_IfLj2EE
    .private_segment_fixed_size: 0
    .sgpr_count:     40
    .sgpr_spill_count: 0
    .symbol:         _Z12giou_partialPK15HIP_vector_typeIfLj4EES2_S2_PKiPS_IfLj2EE.kd
    .uniform_work_group_size: 1
    .uses_dynamic_stack: false
    .vgpr_count:     60
    .vgpr_spill_count: 0
    .wavefront_size: 64
  - .agpr_count:     0
    .args:
      - .actual_access:  read_only
        .address_space:  global
        .offset:         0
        .size:           8
        .value_kind:     global_buffer
      - .actual_access:  write_only
        .address_space:  global
        .offset:         8
        .size:           8
        .value_kind:     global_buffer
    .group_segment_fixed_size: 0
    .kernarg_segment_align: 8
    .kernarg_segment_size: 16
    .language:       OpenCL C
    .language_version:
      - 2
      - 0
    .max_flat_workgroup_size: 64
    .name:           _Z10giou_finalPK15HIP_vector_typeIfLj2EEPf
    .private_segment_fixed_size: 0
    .sgpr_count:     18
    .sgpr_spill_count: 0
    .symbol:         _Z10giou_finalPK15HIP_vector_typeIfLj2EEPf.kd
    .uniform_work_group_size: 1
    .uses_dynamic_stack: false
    .vgpr_count:     18
    .vgpr_spill_count: 0
    .wavefront_size: 64
